# speedup vs baseline: 1.0060x; 1.0060x over previous
.LBB0_4:
	v_lshrrev_b32_e32 v4, 13, v2
	v_lshrrev_b32_e32 v6, 3, v0
	v_ashrrev_i32_e32 v3, 17, v2
	v_and_b32_e32 v4, 14, v4
	v_and_b32_e32 v6, 14, v6
	v_add_u32_e32 v4, v4, v3
	v_add_u32_e32 v6, v3, v6
	s_load_dwordx2 s[2:3], s[0:1], 0x0
	v_ashrrev_i32_e32 v5, 31, v4
	v_ashrrev_i32_e32 v7, 31, v6
	v_lshlrev_b64 v[4:5], 11, v[4:5]
	v_lshlrev_b64 v[6:7], 7, v[6:7]
	v_lshrrev_b32_e32 v1, 7, v2
	v_lshl_add_u64 v[4:5], v[4:5], 0, v[6:7]
	s_movk_i32 s4, 0x7f
	v_and_or_b32 v4, v1, s4, v4
	v_lshlrev_b64 v[4:5], 9, v[4:5]
	v_lshlrev_b32_e32 v0, 5, v0
	s_waitcnt lgkmcnt(0)
	v_lshl_add_u64 v[4:5], s[2:3], 0, v[4:5]
	v_and_b32_e32 v0, 0x1e0, v0
	v_mov_b32_e32 v1, 0
	v_lshl_add_u64 v[0:1], v[4:5], 0, v[0:1]
	global_load_dwordx4 v[4:7], v[0:1], off
	global_load_dwordx4 v[8:11], v[0:1], off offset:16
	s_load_dwordx2 s[0:1], s[0:1], 0x10
	v_ashrrev_i32_e32 v3, 31, v2
	s_waitcnt lgkmcnt(0)
	v_lshl_add_u64 v[0:1], v[2:3], 4, s[0:1]
	s_waitcnt vmcnt(1)
	v_cvt_pk_bf16_f32 v4, v4, v5
	v_cvt_pk_bf16_f32 v5, v6, v7
	s_waitcnt vmcnt(0)
	v_cvt_pk_bf16_f32 v6, v8, v9
	v_cvt_pk_bf16_f32 v7, v10, v11
	global_store_dwordx4 v[0:1], v[4:7], off sc0 sc1
	s_endpgm
